# conv rows: previous/next-row loads issued unconditionally with the row's own loads (one exposed latency per row instead of three)
# speedup vs baseline: 1.0106x; 1.0106x over previous
.LBB0_1894:
	v_lshl_add_u64 v[20:21], s[40:41], 0, v[2:3]
	v_add_co_u32_e32 v4, vcc, 0x44600000, v20
	s_cmpk_lt_i32 s34, 0x4000
	s_nop 0
	v_addc_co_u32_e32 v5, vcc, 0, v21, vcc
	global_load_dwordx4 v[12:15], v[4:5], off offset:1024
	global_load_dwordx4 v[16:19], v[4:5], off offset:2048
	global_load_dwordx4 v[24:27], v[8:9], off offset:2048
	global_load_dwordx4 v[28:31], v[8:9], off offset:2064
	s_nop 0
	global_load_dwordx4 v[4:7], v[4:5], off
	v_add_co_u32_e32 v76, vcc, 0x445ff000, v20
	s_nop 1
	v_addc_co_u32_e32 v77, vcc, 0, v21, vcc
	v_add_co_u32_e32 v78, vcc, 0x44601000, v20
	s_nop 1
	v_addc_co_u32_e32 v79, vcc, 0, v21, vcc
	global_load_dwordx4 v[44:47], v[76:77], off offset:2048
	global_load_dwordx4 v[48:51], v[76:77], off offset:3072
	global_load_dwordx4 v[52:55], v[8:9], off offset:16
	global_load_dwordx4 v[56:59], v[8:9], off
	global_load_dwordx4 v[60:63], v[78:79], off
	global_load_dwordx4 v[64:67], v[78:79], off offset:1024
	global_load_dwordx4 v[68:71], v[10:11], off offset:16
	global_load_dwordx4 v[72:75], v[10:11], off
	s_movk_i32 s1, 0xfff
	s_cselect_b32 s1, s1, 0xff
	s_and_b32 s2, s1, s34
	s_cmp_eq_u32 s2, 0
	s_waitcnt vmcnt(12)
	v_lshlrev_b32_e32 v32, 16, v12
	v_and_b32_e32 v33, 0xffff0000, v12
	s_waitcnt vmcnt(11)
	v_lshlrev_b32_e32 v34, 16, v16
	v_and_b32_e32 v35, 0xffff0000, v16
	v_lshlrev_b32_e32 v12, 16, v13
	v_and_b32_e32 v13, 0xffff0000, v13
	v_lshlrev_b32_e32 v16, 16, v17
	v_and_b32_e32 v17, 0xffff0000, v17
	v_lshlrev_b32_e32 v36, 16, v14
	v_and_b32_e32 v37, 0xffff0000, v14
	v_lshlrev_b32_e32 v38, 16, v18
	v_and_b32_e32 v39, 0xffff0000, v18
	v_lshlrev_b32_e32 v14, 16, v15
	v_and_b32_e32 v15, 0xffff0000, v15
	v_lshlrev_b32_e32 v18, 16, v19
	v_and_b32_e32 v19, 0xffff0000, v19
	v_pk_mul_f32 v[32:33], v[32:33], v[34:35]
	v_pk_mul_f32 v[16:17], v[12:13], v[16:17]
	v_pk_mul_f32 v[34:35], v[36:37], v[38:39]
	v_pk_mul_f32 v[18:19], v[14:15], v[18:19]
	s_waitcnt vmcnt(10)
	v_pk_mul_f32 v[12:13], v[32:33], v[24:25]
	v_pk_mul_f32 v[14:15], v[16:17], v[26:27]
	s_waitcnt vmcnt(9)
	v_pk_mul_f32 v[16:17], v[34:35], v[28:29]
	v_pk_mul_f32 v[18:19], v[18:19], v[30:31]
	s_cbranch_scc1 .LBB0_1896
	s_nop 1
	s_nop 0
	s_nop 0
	s_waitcnt vmcnt(7)
	v_mov_b32_e32 v24, v44
	v_mov_b32_e32 v25, v45
	v_mov_b32_e32 v26, v46
	v_mov_b32_e32 v27, v47
	v_lshlrev_b32_e32 v40, 16, v24
	v_and_b32_e32 v41, 0xffff0000, v24
	s_waitcnt vmcnt(6)
	v_mov_b32_e32 v28, v48
	v_mov_b32_e32 v29, v49
	v_mov_b32_e32 v30, v50
	v_mov_b32_e32 v31, v51
	v_lshlrev_b32_e32 v42, 16, v28
	v_and_b32_e32 v43, 0xffff0000, v28
	v_lshlrev_b32_e32 v24, 16, v25
	v_and_b32_e32 v25, 0xffff0000, v25
	v_lshlrev_b32_e32 v28, 16, v29
	v_and_b32_e32 v29, 0xffff0000, v29
	v_pk_mul_f32 v[24:25], v[24:25], v[28:29]
	v_lshlrev_b32_e32 v28, 16, v30
	s_waitcnt vmcnt(4)
	v_mov_b32_e32 v32, v52
	v_mov_b32_e32 v33, v53
	v_mov_b32_e32 v34, v54
	v_mov_b32_e32 v35, v55
	v_mov_b32_e32 v36, v56
	v_mov_b32_e32 v37, v57
	v_mov_b32_e32 v38, v58
	v_mov_b32_e32 v39, v59
	v_pk_fma_f32 v[14:15], v[24:25], v[38:39], v[14:15]
	v_lshlrev_b32_e32 v24, 16, v26
	v_and_b32_e32 v25, 0xffff0000, v26
	v_and_b32_e32 v29, 0xffff0000, v30
	v_pk_mul_f32 v[24:25], v[24:25], v[28:29]
	v_lshlrev_b32_e32 v26, 16, v31
	v_pk_fma_f32 v[16:17], v[24:25], v[32:33], v[16:17]
	v_lshlrev_b32_e32 v24, 16, v27
	v_and_b32_e32 v25, 0xffff0000, v27
	v_and_b32_e32 v27, 0xffff0000, v31
	v_pk_mul_f32 v[40:41], v[40:41], v[42:43]
	v_pk_mul_f32 v[24:25], v[24:25], v[26:27]
	v_pk_fma_f32 v[12:13], v[40:41], v[36:37], v[12:13]
	v_pk_fma_f32 v[18:19], v[24:25], v[34:35], v[18:19]
.LBB0_1896:
	s_cmp_eq_u32 s2, s1
	s_cbranch_scc1 .LBB0_1893
	s_nop 1
	s_waitcnt vmcnt(3)
	v_mov_b32_e32 v24, v60
	v_mov_b32_e32 v25, v61
	v_mov_b32_e32 v26, v62
	v_mov_b32_e32 v27, v63
	v_lshlrev_b32_e32 v20, 16, v24
	v_and_b32_e32 v21, 0xffff0000, v24
	s_waitcnt vmcnt(2)
	v_mov_b32_e32 v28, v64
	v_mov_b32_e32 v29, v65
	v_mov_b32_e32 v30, v66
	v_mov_b32_e32 v31, v67
	v_lshlrev_b32_e32 v40, 16, v28
	v_and_b32_e32 v41, 0xffff0000, v28
	v_pk_mul_f32 v[20:21], v[20:21], v[40:41]
	v_lshlrev_b32_e32 v24, 16, v29
	s_waitcnt vmcnt(0)
	v_mov_b32_e32 v32, v68
	v_mov_b32_e32 v33, v69
	v_mov_b32_e32 v34, v70
	v_mov_b32_e32 v35, v71
	v_mov_b32_e32 v36, v72
	v_mov_b32_e32 v37, v73
	v_mov_b32_e32 v38, v74
	v_mov_b32_e32 v39, v75
	v_pk_fma_f32 v[12:13], v[20:21], v[36:37], v[12:13]
	v_lshlrev_b32_e32 v20, 16, v25
	v_and_b32_e32 v21, 0xffff0000, v25
	v_and_b32_e32 v25, 0xffff0000, v29
	v_pk_mul_f32 v[20:21], v[20:21], v[24:25]
	v_lshlrev_b32_e32 v24, 16, v30
	v_pk_fma_f32 v[14:15], v[20:21], v[38:39], v[14:15]
	v_lshlrev_b32_e32 v20, 16, v26
	v_and_b32_e32 v21, 0xffff0000, v26
	v_and_b32_e32 v25, 0xffff0000, v30
	v_pk_mul_f32 v[20:21], v[20:21], v[24:25]
	v_lshlrev_b32_e32 v24, 16, v31
	v_pk_fma_f32 v[16:17], v[20:21], v[32:33], v[16:17]
	v_lshlrev_b32_e32 v20, 16, v27
	v_and_b32_e32 v21, 0xffff0000, v27
	v_and_b32_e32 v25, 0xffff0000, v31
	v_pk_mul_f32 v[20:21], v[20:21], v[24:25]
	s_nop 0
	v_pk_fma_f32 v[18:19], v[20:21], v[34:35], v[18:19]
	s_branch .LBB0_1893
